# v71 + counted vmcnt(8) at S5 unit head (allow the 8 epilogue stores in flight) + attention unit-1 prologue drain moved to the entry path only
# speedup vs baseline: 1.0063x; 1.0055x over previous
.LBB0_677:
	v_readlane_b32 s0, v249, 34
	v_readlane_b32 s1, v249, 35
	v_readlane_b32 s69, v251, 3
	s_andn2_b64 vcc, exec, s[0:1]
	s_mov_b32 s68, s69
	s_waitcnt vmcnt(0)
	s_cbranch_vccz .LBB0_681

.LBB0_681:
	s_ashr_i32 s48, s69, 5
	v_mov_b32_e32 v3, v0
	s_barrier
	s_ashr_i32 s49, s48, 31
	v_readfirstlane_b32 s0, v3
	s_bfe_u32 s70, s69, 0x30002
	s_ashr_i32 s12, s0, 6
	s_lshl_b64 s[0:1], s[48:49], 3
	s_or_b32 s0, s0, s70
	s_and_b32 s66, s69, 3
	s_lshl_b64 s[40:41], s[0:1], 17
	s_lshl_b64 s[38:39], s[0:1], 18
	s_add_u32 s50, s10, s38
	s_addc_u32 s51, s11, s39
	s_sub_u32 s0, 0, s40
	s_subb_u32 s1, 0, s41
	s_add_u32 s52, s50, s0
	s_addc_u32 s53, s51, s1
	s_lshl_b32 s0, s66, 8
	s_lshl_b32 s20, s12, 5
	v_and_b32_e32 v156, 31, v3
	s_add_i32 s20, s20, s0
	v_or_b32_e32 v134, s20, v156
	v_ashrrev_i32_e32 v135, 31, v134
	v_bfe_u32 v158, v3, 5, 1
	v_lshlrev_b64 v[4:5], 6, v[134:135]
	v_lshlrev_b64 v[6:7], 7, v[134:135]
	v_lshl_add_u64 v[4:5], s[52:53], 0, v[4:5]
	v_lshl_add_u64 v[6:7], s[50:51], 0, v[6:7]
	v_lshlrev_b32_e32 v12, 4, v158
	v_mov_b32_e32 v13, v2
	v_lshl_add_u64 v[6:7], v[6:7], 0, v[12:13]
	v_lshl_add_u64 v[4:5], v[4:5], 0, v[12:13]
	s_brev_b32 s0, 64
	global_load_dwordx4 v[98:101], v[6:7], off
	global_load_dwordx4 v[102:105], v[6:7], off offset:32
	global_load_dwordx4 v[106:109], v[6:7], off offset:64
	global_load_dwordx4 v[110:113], v[6:7], off offset:96
	v_add_co_u32_e32 v4, vcc, s0, v4
	s_lshl_b64 s[0:1], s[48:49], 17
	s_nop 0
	v_addc_co_u32_e32 v5, vcc, 0, v5, vcc
	global_load_dwordx4 v[114:117], v[4:5], off
	global_load_dwordx4 v[118:121], v[4:5], off offset:32
	v_readlane_b32 s18, v251, 55
	v_readlane_b32 s19, v251, 56
	s_add_u32 s42, s18, s0
	s_addc_u32 s43, s19, s1
	v_readlane_b32 s0, v251, 51
	s_add_u32 s40, s0, s38
	s_mov_b32 s0, 0x2aaaaaab
	v_mul_hi_i32 v4, v3, s0
	v_lshrrev_b32_e32 v5, 31, v4
	v_ashrrev_i32_e32 v4, 1, v4
	v_add_u32_e32 v13, v4, v5
	v_mul_lo_u32 v4, v13, 12
	v_readlane_b32 s1, v251, 52
	v_sub_u32_e32 v18, v3, v4
	s_addc_u32 s41, s1, s39
	v_cmp_lt_i32_e32 vcc, 7, v18
	v_lshlrev_b32_e32 v4, 3, v18
	s_and_saveexec_b64 s[0:1], vcc
	s_xor_b64 s[0:1], exec, s[0:1]
	v_lshlrev_b32_e32 v6, 5, v13
	v_ashrrev_i32_e32 v7, 31, v6
	v_lshl_add_u64 v[6:7], v[6:7], 1, s[42:43]
	v_mov_b32_e32 v5, v2
	s_movk_i32 s18, 0xff80
	v_lshl_add_u64 v[4:5], v[4:5], 1, v[6:7]
	s_mov_b32 s19, -1
	v_lshl_add_u64 v[82:83], v[4:5], 0, s[18:19]
	s_or_saveexec_b64 s[0:1], s[0:1]
	v_mov_b64_e32 v[84:85], 0x800
	s_xor_b64 exec, exec, s[0:1]
	v_lshlrev_b32_e32 v6, 6, v13
	v_ashrrev_i32_e32 v7, 31, v6
	v_lshl_add_u64 v[6:7], v[6:7], 1, s[40:41]
	v_ashrrev_i32_e32 v5, 31, v4
	v_lshl_add_u64 v[82:83], v[4:5], 1, v[6:7]
	v_mov_b64_e32 v[84:85], 0x1000
	s_or_b64 exec, exec, s[0:1]
	v_add_u32_e32 v4, 0x200, v3
	s_mov_b32 s0, 0x2aaaaaab
	v_mul_hi_i32 v5, v4, s0
	v_lshrrev_b32_e32 v6, 31, v5
	v_ashrrev_i32_e32 v5, 1, v5
	v_add_u32_e32 v19, v5, v6
	v_mul_lo_u32 v5, v19, 12
	v_sub_u32_e32 v20, v4, v5
	v_cmp_lt_i32_e32 vcc, 7, v20
	v_lshlrev_b32_e32 v4, 3, v20
	s_and_saveexec_b64 s[0:1], vcc
	s_xor_b64 s[0:1], exec, s[0:1]
	v_lshlrev_b32_e32 v6, 5, v19
	v_ashrrev_i32_e32 v7, 31, v6
	v_lshl_add_u64 v[6:7], v[6:7], 1, s[42:43]
	v_mov_b32_e32 v5, v2
	s_movk_i32 s18, 0xff80
	v_lshl_add_u64 v[4:5], v[4:5], 1, v[6:7]
	s_mov_b32 s19, -1
	v_lshl_add_u64 v[86:87], v[4:5], 0, s[18:19]
	s_or_saveexec_b64 s[0:1], s[0:1]
	v_mov_b64_e32 v[88:89], 0x800
	s_xor_b64 exec, exec, s[0:1]
	v_lshlrev_b32_e32 v6, 6, v19
	v_ashrrev_i32_e32 v7, 31, v6
	v_lshl_add_u64 v[6:7], v[6:7], 1, s[40:41]
	v_ashrrev_i32_e32 v5, 31, v4
	v_lshl_add_u64 v[86:87], v[4:5], 1, v[6:7]
	v_mov_b64_e32 v[88:89], 0x1000
	s_or_b64 exec, exec, s[0:1]
	global_load_dwordx4 v[8:11], v[82:83], off
	s_movk_i32 s0, 0xff
	v_cmp_lt_i32_e32 vcc, s0, v3
	s_movk_i32 s0, 0x100
	v_cmp_gt_i32_e64 s[0:1], s0, v3
	s_and_saveexec_b64 s[54:55], s[0:1]
	s_cbranch_execz .LBB0_691
	global_load_dwordx4 v[122:125], v[86:87], off

.LBB0_781:
	s_ashr_i32 s40, s52, 5
	s_and_b32 s53, s52, 31
	s_lshl_b32 s1, s40, 7
	s_lshl_b32 s0, s53, 11
	s_ashr_i32 s12, s1, 31
	s_add_u32 s0, s0, s1
	s_addc_u32 s1, 0, s12
	s_lshl_b64 s[0:1], s[0:1], 9
	s_add_u32 s0, s8, s0
	s_waitcnt vmcnt(8)
	v_mov_b32_e32 v36, v0
	s_addc_u32 s1, s9, s1
	s_lshl_b32 s12, s53, 16
	v_mov_b32_e32 v56, v0
	s_barrier
	s_add_u32 s12, s48, s12
	s_addc_u32 s39, s49, 0
	v_readfirstlane_b32 s38, v56
	s_ashr_i32 s41, s38, 6
	s_cmp_lt_i32 s41, 8
	s_cselect_b32 s42, s41, 7
	s_ashr_i32 s43, s42, 31
	s_waitcnt vmcnt(8)
	v_ashrrev_i32_e32 v4, 4, v56
	s_lshl_b64 s[42:43], s[42:43], 13
	v_lshlrev_b32_e32 v6, 3, v56
	v_xor_b32_e32 v7, v4, v56
	s_add_u32 s42, s12, s42
	v_and_b32_e32 v5, 63, v56
	v_and_b32_e32 v22, 0x78, v6
	v_lshlrev_b32_e32 v6, 8, v4
	v_lshlrev_b32_e32 v7, 4, v7
	s_addc_u32 s43, s39, s43
	v_and_or_b32 v57, v7, s84, v6
	v_lshlrev_b32_e32 v6, 4, v5
	v_mov_b32_e32 v7, v2
	v_readlane_b32 s12, v249, 38
	v_ashrrev_i32_e32 v5, 31, v4
	v_lshl_add_u64 v[54:55], s[42:43], 0, v[6:7]
	v_or_b32_e32 v6, s12, v22
	v_lshlrev_b64 v[4:5], 9, v[4:5]
	v_lshl_add_u64 v[20:21], s[0:1], 0, v[4:5]
	v_lshlrev_b32_e32 v16, 1, v6
	v_mov_b32_e32 v17, v2
	s_mov_b64 s[42:43], 0x4000
	v_lshl_add_u64 v[70:71], v[20:21], 0, v[16:17]
	v_lshl_add_u64 v[24:25], v[20:21], 0, s[42:43]
	s_mov_b64 s[42:43], 0x8000
	global_load_dwordx4 v[4:7], v[70:71], off
	v_lshl_add_u64 v[74:75], v[24:25], 0, v[16:17]
	v_lshl_add_u64 v[28:29], v[20:21], 0, s[42:43]
	s_mov_b64 s[42:43], 0xc000
	global_load_dwordx4 v[8:11], v[74:75], off
	v_lshl_add_u64 v[94:95], v[28:29], 0, v[16:17]
	v_lshl_add_u64 v[32:33], v[20:21], 0, s[42:43]
	global_load_dwordx4 v[12:15], v[94:95], off
	v_lshl_add_u64 v[98:99], v[32:33], 0, v[16:17]
	global_load_dwordx4 v[16:19], v[98:99], off
	v_readlane_b32 s12, v249, 39
	v_readlane_b32 s18, v248, 11
	v_readlane_b32 s19, v248, 12
	v_or_b32_e32 v22, s12, v22
	v_lshlrev_b32_e32 v34, 1, v22
	v_mov_b32_e32 v35, v2
	s_mov_b32 s19, s21
	v_lshl_add_u64 v[20:21], v[20:21], 0, v[34:35]
	v_lshl_add_u64 v[24:25], v[24:25], 0, v[34:35]
	v_lshl_add_u64 v[28:29], v[28:29], 0, v[34:35]
	v_lshl_add_u64 v[32:33], v[32:33], 0, v[34:35]
	v_lshl_add_u64 v[50:51], v[54:55], 0, s[18:19]
	global_load_dwordx4 v[20:23], v[20:21], off
	s_mov_b32 s12, s18
	global_load_dwordx4 v[24:27], v[24:25], off
	v_writelane_b32 v248, s12, 11
	global_load_dwordx4 v[28:31], v[28:29], off
	v_and_b32_e32 v3, 15, v56
	global_load_dwordx4 v[32:35], v[32:33], off
	s_nop 0
	global_load_dwordx4 v[38:41], v[50:51], off
	global_load_dwordx4 v[42:45], v[50:51], off offset:1024
	global_load_dwordx4 v[46:49], v[50:51], off offset:2048
	s_nop 0
	global_load_dwordx4 v[50:53], v[50:51], off offset:3072
	v_writelane_b32 v248, s13, 12
	v_bfe_u32 v37, v56, 4, 2
	v_add_u32_e32 v120, 0, v57
	v_readlane_b32 s18, v248, 13
	v_readlane_b32 s19, v248, 14
	v_lshl_add_u32 v121, v3, 8, 0
	s_mov_b32 s19, s21
	v_lshl_add_u64 v[118:119], v[54:55], 0, s[18:19]
	s_mov_b32 s12, s18
	v_writelane_b32 v248, s12, 13
	s_cmp_gt_i32 s41, 7
	s_waitcnt vmcnt(11)
	ds_write_b128 v120, v[4:7]
	s_waitcnt vmcnt(10)
	ds_write_b128 v120, v[8:11] offset:8192
	s_waitcnt vmcnt(9)
	ds_write_b128 v120, v[12:15] offset:16384
	s_waitcnt vmcnt(8)
	ds_write_b128 v120, v[16:19] offset:24576
	v_bitop3_b32 v4, v37, v56, 15 bitop3:0x78
	v_lshl_add_u32 v122, v4, 4, v121
	s_waitcnt lgkmcnt(0)
	s_barrier
	ds_read_b128 v[4:7], v122
	ds_read_b128 v[8:11], v122 offset:4096
	ds_read_b128 v[12:15], v122 offset:8192
	ds_read_b128 v[16:19], v122 offset:12288
	ds_read_b128 v[54:57], v122 offset:16384
	ds_read_b128 v[58:61], v122 offset:20480
	ds_read_b128 v[62:65], v122 offset:24576
	ds_read_b128 v[66:69], v122 offset:28672
	v_writelane_b32 v248, s13, 14
	global_load_dwordx4 v[70:73], v[70:71], off
	s_nop 0
	global_load_dwordx4 v[74:77], v[74:75], off
	s_waitcnt vmcnt(5) lgkmcnt(7)
	v_mfma_f32_16x16x32_bf16 v[4:7], v[38:41], v[4:7], 0
	s_waitcnt lgkmcnt(6)
	v_mfma_f32_16x16x32_bf16 v[8:11], v[38:41], v[8:11], 0
	s_waitcnt lgkmcnt(5)
	v_mfma_f32_16x16x32_bf16 v[12:15], v[38:41], v[12:15], 0
	s_waitcnt lgkmcnt(4)
	v_mfma_f32_16x16x32_bf16 v[16:19], v[38:41], v[16:19], 0
	v_bitop3_b32 v78, v37, v3, 4 bitop3:0x36
	v_lshl_add_u32 v123, v78, 4, v121
	ds_read_b128 v[78:81], v123
	ds_read_b128 v[82:85], v123 offset:4096
	ds_read_b128 v[86:89], v123 offset:8192
	ds_read_b128 v[90:93], v123 offset:12288
	global_load_dwordx4 v[94:97], v[94:95], off
	s_nop 0
	global_load_dwordx4 v[98:101], v[98:99], off
	s_waitcnt lgkmcnt(7)
	v_mfma_f32_16x16x32_bf16 v[54:57], v[38:41], v[54:57], 0
	s_waitcnt lgkmcnt(6)
	v_mfma_f32_16x16x32_bf16 v[58:61], v[38:41], v[58:61], 0
	s_waitcnt lgkmcnt(5)
	v_mfma_f32_16x16x32_bf16 v[62:65], v[38:41], v[62:65], 0
	s_waitcnt lgkmcnt(4)
	v_mfma_f32_16x16x32_bf16 v[38:41], v[38:41], v[66:69], 0
	ds_read_b128 v[66:69], v123 offset:16384
	ds_read_b128 v[102:105], v123 offset:20480
	ds_read_b128 v[106:109], v123 offset:24576
	ds_read_b128 v[110:113], v123 offset:28672
	global_load_dwordx4 v[114:117], v[118:119], off
	ds_write_b128 v120, v[20:23] offset:32768
	s_waitcnt vmcnt(7) lgkmcnt(8)
	v_mfma_f32_16x16x32_bf16 v[4:7], v[42:45], v[78:81], v[4:7]
	s_waitcnt lgkmcnt(7)
	v_mfma_f32_16x16x32_bf16 v[8:11], v[42:45], v[82:85], v[8:11]
	s_waitcnt lgkmcnt(6)
	v_mfma_f32_16x16x32_bf16 v[12:15], v[42:45], v[86:89], v[12:15]
	s_waitcnt lgkmcnt(5)
	v_mfma_f32_16x16x32_bf16 v[16:19], v[42:45], v[90:93], v[16:19]
	v_bitop3_b32 v20, v37, v3, 8 bitop3:0x36
	v_lshl_add_u32 v124, v20, 4, v121
	ds_read_b128 v[20:23], v124
	ds_read_b128 v[78:81], v124 offset:4096
	ds_read_b128 v[82:85], v124 offset:8192
	ds_read_b128 v[86:89], v124 offset:12288
	global_load_dwordx4 v[90:93], v[118:119], off offset:1024
	ds_write_b128 v120, v[24:27] offset:40960
	s_waitcnt lgkmcnt(9)
	v_mfma_f32_16x16x32_bf16 v[24:27], v[42:45], v[66:69], v[54:57]
	s_waitcnt lgkmcnt(8)
	v_mfma_f32_16x16x32_bf16 v[54:57], v[42:45], v[102:105], v[58:61]
	s_waitcnt lgkmcnt(7)
	v_mfma_f32_16x16x32_bf16 v[58:61], v[42:45], v[106:109], v[62:65]
	s_waitcnt lgkmcnt(6)
	v_mfma_f32_16x16x32_bf16 v[38:41], v[42:45], v[110:113], v[38:41]
	ds_read_b128 v[42:45], v124 offset:16384
	ds_read_b128 v[62:65], v124 offset:20480
	ds_read_b128 v[66:69], v124 offset:24576
	ds_read_b128 v[102:105], v124 offset:28672
	global_load_dwordx4 v[106:109], v[118:119], off offset:2048
	ds_write_b128 v120, v[28:31] offset:49152
	s_waitcnt vmcnt(8) lgkmcnt(9)
	v_mfma_f32_16x16x32_bf16 v[4:7], v[46:49], v[20:23], v[4:7]
	s_waitcnt lgkmcnt(8)
	v_mfma_f32_16x16x32_bf16 v[8:11], v[46:49], v[78:81], v[8:11]
	s_waitcnt lgkmcnt(7)
	v_mfma_f32_16x16x32_bf16 v[12:15], v[46:49], v[82:85], v[12:15]
	s_waitcnt lgkmcnt(6)
	v_mfma_f32_16x16x32_bf16 v[16:19], v[46:49], v[86:89], v[16:19]
	v_bitop3_b32 v20, v37, v3, 12 bitop3:0x36
	v_lshl_add_u32 v110, v20, 4, v121
	ds_read_b128 v[20:23], v110
	ds_read_b128 v[28:31], v110 offset:4096
	ds_read_b128 v[78:81], v110 offset:8192
	ds_read_b128 v[82:85], v110 offset:12288
	global_load_dwordx4 v[86:89], v[118:119], off offset:3072
	ds_write_b128 v120, v[32:35] offset:57344
	s_waitcnt lgkmcnt(9)
	v_mfma_f32_16x16x32_bf16 v[24:27], v[46:49], v[42:45], v[24:27]
	s_waitcnt lgkmcnt(8)
	v_mfma_f32_16x16x32_bf16 v[32:35], v[46:49], v[62:65], v[54:57]
	s_waitcnt lgkmcnt(7)
	v_mfma_f32_16x16x32_bf16 v[42:45], v[46:49], v[66:69], v[58:61]
	s_waitcnt lgkmcnt(6)
	v_mfma_f32_16x16x32_bf16 v[38:41], v[46:49], v[102:105], v[38:41]
	ds_read_b128 v[46:49], v110 offset:16384
	ds_read_b128 v[54:57], v110 offset:20480
	ds_read_b128 v[58:61], v110 offset:24576
	ds_read_b128 v[62:65], v110 offset:28672
	s_waitcnt vmcnt(8) lgkmcnt(8)
	v_mfma_f32_16x16x32_bf16 v[4:7], v[50:53], v[20:23], v[4:7]
	s_waitcnt lgkmcnt(7)
	v_mfma_f32_16x16x32_bf16 v[8:11], v[50:53], v[28:31], v[8:11]
	s_waitcnt lgkmcnt(6)
	v_mfma_f32_16x16x32_bf16 v[12:15], v[50:53], v[78:81], v[12:15]
	s_waitcnt lgkmcnt(5)
	v_mfma_f32_16x16x32_bf16 v[16:19], v[50:53], v[82:85], v[16:19]
	s_waitcnt lgkmcnt(3)
	v_mfma_f32_16x16x32_bf16 v[20:23], v[50:53], v[46:49], v[24:27]
	s_waitcnt lgkmcnt(2)
	v_mfma_f32_16x16x32_bf16 v[24:27], v[50:53], v[54:57], v[32:35]
	s_waitcnt lgkmcnt(1)
	v_mfma_f32_16x16x32_bf16 v[28:31], v[50:53], v[58:61], v[42:45]
	s_waitcnt lgkmcnt(0)
	v_mfma_f32_16x16x32_bf16 v[32:35], v[50:53], v[62:65], v[38:41]
	s_barrier
	s_nop 1
	ds_read_b128 v[38:41], v122 offset:32768
	ds_read_b128 v[42:45], v122 offset:36864
	ds_read_b128 v[46:49], v122 offset:40960
	ds_read_b128 v[50:53], v122 offset:45056
	ds_read_b128 v[54:57], v122 offset:49152
	ds_read_b128 v[58:61], v122 offset:53248
	ds_read_b128 v[62:65], v122 offset:57344
	ds_read_b128 v[66:69], v122 offset:61440
	s_waitcnt vmcnt(3) lgkmcnt(7)
	v_mfma_f32_16x16x32_bf16 v[4:7], v[114:117], v[38:41], v[4:7]
	s_waitcnt lgkmcnt(6)
	v_mfma_f32_16x16x32_bf16 v[8:11], v[114:117], v[42:45], v[8:11]
	s_waitcnt lgkmcnt(5)
	v_mfma_f32_16x16x32_bf16 v[12:15], v[114:117], v[46:49], v[12:15]
	s_waitcnt lgkmcnt(4)
	v_mfma_f32_16x16x32_bf16 v[16:19], v[114:117], v[50:53], v[16:19]
	ds_read_b128 v[38:41], v123 offset:32768
	ds_read_b128 v[42:45], v123 offset:36864
	ds_read_b128 v[46:49], v123 offset:40960
	ds_read_b128 v[50:53], v123 offset:45056
	s_waitcnt lgkmcnt(7)
	v_mfma_f32_16x16x32_bf16 v[20:23], v[114:117], v[54:57], v[20:23]
	s_waitcnt lgkmcnt(6)
	v_mfma_f32_16x16x32_bf16 v[24:27], v[114:117], v[58:61], v[24:27]
	s_waitcnt lgkmcnt(5)
	v_mfma_f32_16x16x32_bf16 v[28:31], v[114:117], v[62:65], v[28:31]
	s_waitcnt lgkmcnt(4)
	v_mfma_f32_16x16x32_bf16 v[32:35], v[114:117], v[66:69], v[32:35]
	ds_read_b128 v[54:57], v123 offset:49152
	ds_read_b128 v[58:61], v123 offset:53248
	ds_read_b128 v[62:65], v123 offset:57344
	ds_read_b128 v[66:69], v123 offset:61440
	ds_write_b128 v120, v[70:73]
	s_waitcnt vmcnt(2) lgkmcnt(8)
	v_mfma_f32_16x16x32_bf16 v[4:7], v[90:93], v[38:41], v[4:7]
	s_waitcnt lgkmcnt(7)
	v_mfma_f32_16x16x32_bf16 v[8:11], v[90:93], v[42:45], v[8:11]
	s_waitcnt lgkmcnt(6)
	v_mfma_f32_16x16x32_bf16 v[12:15], v[90:93], v[46:49], v[12:15]
	s_waitcnt lgkmcnt(5)
	v_mfma_f32_16x16x32_bf16 v[16:19], v[90:93], v[50:53], v[16:19]
	ds_read_b128 v[38:41], v124 offset:32768
	ds_read_b128 v[42:45], v124 offset:36864
	ds_read_b128 v[46:49], v124 offset:40960
	ds_read_b128 v[50:53], v124 offset:45056
	ds_write_b128 v120, v[74:77] offset:8192
	s_waitcnt lgkmcnt(9)
	v_mfma_f32_16x16x32_bf16 v[20:23], v[90:93], v[54:57], v[20:23]
	s_waitcnt lgkmcnt(8)
	v_mfma_f32_16x16x32_bf16 v[24:27], v[90:93], v[58:61], v[24:27]
	s_waitcnt lgkmcnt(7)
	v_mfma_f32_16x16x32_bf16 v[28:31], v[90:93], v[62:65], v[28:31]
	s_waitcnt lgkmcnt(6)
	v_mfma_f32_16x16x32_bf16 v[32:35], v[90:93], v[66:69], v[32:35]
	ds_read_b128 v[54:57], v124 offset:49152
	ds_read_b128 v[58:61], v124 offset:53248
	ds_read_b128 v[62:65], v124 offset:57344
	ds_read_b128 v[66:69], v124 offset:61440
	ds_write_b128 v120, v[94:97] offset:16384
	s_waitcnt vmcnt(1) lgkmcnt(9)
	v_mfma_f32_16x16x32_bf16 v[4:7], v[106:109], v[38:41], v[4:7]
	s_waitcnt lgkmcnt(8)
	v_mfma_f32_16x16x32_bf16 v[8:11], v[106:109], v[42:45], v[8:11]
	s_waitcnt lgkmcnt(7)
	v_mfma_f32_16x16x32_bf16 v[12:15], v[106:109], v[46:49], v[12:15]
	s_waitcnt lgkmcnt(6)
	v_mfma_f32_16x16x32_bf16 v[16:19], v[106:109], v[50:53], v[16:19]
	ds_read_b128 v[38:41], v110 offset:32768
	ds_read_b128 v[42:45], v110 offset:36864
	ds_read_b128 v[46:49], v110 offset:40960
	ds_read_b128 v[50:53], v110 offset:45056
	ds_write_b128 v120, v[98:101] offset:24576
	s_waitcnt lgkmcnt(9)
	v_mfma_f32_16x16x32_bf16 v[20:23], v[106:109], v[54:57], v[20:23]
	s_waitcnt lgkmcnt(8)
	v_mfma_f32_16x16x32_bf16 v[54:57], v[106:109], v[58:61], v[24:27]
	s_waitcnt lgkmcnt(7)
	v_mfma_f32_16x16x32_bf16 v[58:61], v[106:109], v[62:65], v[28:31]
	s_waitcnt lgkmcnt(6)
	v_mfma_f32_16x16x32_bf16 v[62:65], v[106:109], v[66:69], v[32:35]
	ds_read_b128 v[66:69], v110 offset:49152
	ds_read_b128 v[70:73], v110 offset:53248
	ds_read_b128 v[74:77], v110 offset:57344
	ds_read_b128 v[78:81], v110 offset:61440
	s_waitcnt vmcnt(0) lgkmcnt(8)
	v_mfma_f32_16x16x32_bf16 v[32:35], v[86:89], v[38:41], v[4:7]
	s_waitcnt lgkmcnt(7)
	v_mfma_f32_16x16x32_bf16 v[28:31], v[86:89], v[42:45], v[8:11]
	s_waitcnt lgkmcnt(6)
	v_mfma_f32_16x16x32_bf16 v[24:27], v[86:89], v[46:49], v[12:15]
	s_waitcnt lgkmcnt(5)
	v_mfma_f32_16x16x32_bf16 v[16:19], v[86:89], v[50:53], v[16:19]
	s_waitcnt lgkmcnt(3)
	v_mfma_f32_16x16x32_bf16 v[20:23], v[86:89], v[66:69], v[20:23]
	s_waitcnt lgkmcnt(2)
	v_mfma_f32_16x16x32_bf16 v[12:15], v[86:89], v[70:73], v[54:57]
	s_waitcnt lgkmcnt(1)
	v_mfma_f32_16x16x32_bf16 v[8:11], v[86:89], v[74:77], v[58:61]
	s_waitcnt lgkmcnt(0)
	v_mfma_f32_16x16x32_bf16 v[4:7], v[86:89], v[78:81], v[62:65]
	s_cbranch_scc1 .LBB0_783
	s_andn2_b32 s38, s38, 63
	s_add_i32 s12, s38, 0
	v_lshlrev_b32_e32 v3, 9, v3
	v_lshlrev_b32_e32 v37, 4, v37
	s_add_i32 s38, s12, 0x10000
	v_add3_u32 v38, s38, v3, v37
	s_add_i32 s38, s12, 0x12000
	ds_write_b128 v38, v[32:35]
	v_add3_u32 v32, s38, v3, v37
	s_add_i32 s38, s12, 0x14000
	ds_write_b128 v32, v[28:31]
	v_add3_u32 v28, s38, v3, v37
	s_add_i32 s38, s12, 0x16000
	ds_write_b128 v28, v[24:27]
	v_add3_u32 v24, s38, v3, v37
	s_add_i32 s38, s12, 0x18000
	ds_write_b128 v24, v[16:19]
	v_add3_u32 v16, s38, v3, v37
	s_add_i32 s38, s12, 0x1a000
	ds_write_b128 v16, v[20:23]
	v_add3_u32 v16, s38, v3, v37
	s_add_i32 s38, s12, 0x1c000
	s_add_i32 s12, s12, 0x1e000
	ds_write_b128 v16, v[12:15]
	v_add3_u32 v12, s38, v3, v37
	v_add3_u32 v3, s12, v3, v37
	ds_write_b128 v12, v[8:11]
	ds_write_b128 v3, v[4:7]
